# SGU: LayerNorm gain/bias quads of a unit requested at the top of its loop iteration instead of behind the second workgroup barrier (exposed L2 round trip per unit)
# baseline (speedup 1.0000x reference)
.LBB0_1962:
	global_load_dwordx4 v[92:95], v[0:1], off nt
	global_load_dwordx4 v[88:91], v[2:3], off nt
	global_load_dwordx4 v[84:87], v[4:5], off nt
	global_load_dwordx4 v[80:83], v[6:7], off nt
	global_load_dwordx4 v[76:79], v[8:9], off nt
	global_load_dwordx4 v[72:75], v[10:11], off nt
	global_load_dwordx4 v[68:71], v[12:13], off nt
	global_load_dwordx4 v[64:67], v[14:15], off nt
	s_and_b32 s30, s42, 7
	v_lshl_or_b32 v244, s30, 8, v159
	v_lshlrev_b32_e32 v244, 2, v244
	v_readlane_b32 s100, v249, 30
	v_readlane_b32 s101, v249, 31
	v_readlane_b32 s30, v249, 32
	v_readlane_b32 s31, v249, 33
	s_nop 4
	global_load_dwordx4 v[228:231], v244, s[100:101]
	global_load_dwordx4 v[232:235], v244, s[30:31]
	global_load_dwordx4 v[236:239], v244, s[100:101] offset:16
	global_load_dwordx4 v[240:243], v244, s[30:31] offset:16
	s_waitcnt vmcnt(12)
	v_add_f32_e32 v0, v60, v62
	v_add_f32_e32 v0, 0, v0
	v_add_f32_e32 v1, v61, v63
	v_add_f32_e32 v2, v56, v58
	v_add_f32_e32 v1, 0, v1
	v_add_f32_e32 v0, v2, v0
	v_add_f32_e32 v2, v57, v59
	v_add_f32_e32 v1, v2, v1
	v_add_f32_e32 v2, v52, v54
	v_add_f32_e32 v0, v2, v0
	v_add_f32_e32 v2, v53, v55
	v_add_f32_e32 v1, v2, v1
	v_add_f32_e32 v2, v48, v50
	v_add_f32_e32 v0, v2, v0
	v_add_f32_e32 v2, v49, v51
	v_add_f32_e32 v2, v2, v1
	ds_bpermute_b32 v3, v160, v0
	ds_bpermute_b32 v4, v160, v2
	s_waitcnt lgkmcnt(0)
	s_barrier
	v_add_f32_e32 v0, v0, v3
	v_add_f32_e32 v2, v2, v4
	ds_bpermute_b32 v1, v161, v0
	ds_bpermute_b32 v3, v161, v2
	s_and_saveexec_b64 s[30:31], s[0:1]
	s_cbranch_execz .LBB0_1964
	s_waitcnt lgkmcnt(1)
	v_add_f32_e32 v0, v0, v1
	v_mul_f32_e32 v0, 0x3a000000, v0
	s_waitcnt lgkmcnt(0)
	v_add_f32_e32 v2, v2, v3
	v_mul_f32_e32 v1, v0, v0
	v_fma_f32 v1, v2, s38, -v1
	v_max_f32_e32 v1, 0, v1
	v_add_f32_e32 v1, 0x3727c5ac, v1
	v_mul_f32_e32 v2, 0x4f800000, v1
	v_cmp_gt_f32_e32 vcc, s39, v1
	s_nop 1
	v_cndmask_b32_e32 v1, v1, v2, vcc
	v_sqrt_f32_e32 v2, v1
	s_nop 0
	v_add_u32_e32 v3, -1, v2
	v_fma_f32 v4, -v3, v2, v1
	v_cmp_ge_f32_e64 s[6:7], 0, v4
	v_add_u32_e32 v4, 1, v2
	s_nop 0
	v_cndmask_b32_e64 v3, v2, v3, s[6:7]
	v_fma_f32 v2, -v4, v2, v1
	v_cmp_lt_f32_e64 s[6:7], 0, v2
	s_nop 1
	v_cndmask_b32_e64 v2, v3, v4, s[6:7]
	v_mul_f32_e32 v3, 0x37800000, v2
	v_cndmask_b32_e32 v2, v2, v3, vcc
	v_cmp_class_f32_e32 vcc, v1, v197
	s_nop 1
	v_cndmask_b32_e32 v1, v2, v1, vcc
	v_div_scale_f32 v2, s[6:7], v1, v1, 1.0
	v_rcp_f32_e32 v3, v2
	s_nop 0
	v_fma_f32 v4, -v2, v3, 1.0
	v_fmac_f32_e32 v3, v4, v3
	v_div_scale_f32 v4, vcc, 1.0, v1, 1.0
	v_mul_f32_e32 v5, v4, v3
	v_fma_f32 v6, -v2, v5, v4
	v_fmac_f32_e32 v5, v6, v3
	v_fma_f32 v2, -v2, v5, v4
	v_div_fmas_f32 v2, v2, v3, v5
	v_div_fixup_f32 v1, v2, v1, 1.0
	ds_write_b64 v196, v[0:1]

.LBB0_1968:
	v_readlane_b32 s52, v249, 18
	v_lshl_or_b32 v132, s30, 8, v159
	v_readlane_b32 s60, v249, 26
	v_readlane_b32 s61, v249, 27
	v_readlane_b32 s62, v249, 28
	v_readlane_b32 s63, v249, 29
	v_readlane_b32 s64, v249, 30
	v_readlane_b32 s65, v249, 31
	v_lshlrev_b32_e32 v4, 2, v132
	v_readlane_b32 s66, v249, 32
	v_readlane_b32 s67, v249, 33
	s_mov_b64 s[60:61], s[64:65]
	s_waitcnt lgkmcnt(0)
	s_barrier
	s_mov_b64 s[62:63], s[66:67]
	s_waitcnt vmcnt(0)
	v_mov_b64_e32 v[8:9], v[228:229]
	v_mov_b64_e32 v[10:11], v[230:231]
	v_mov_b64_e32 v[12:13], v[232:233]
	v_mov_b64_e32 v[14:15], v[234:235]
	v_mov_b64_e32 v[0:1], v[236:237]
	v_mov_b64_e32 v[2:3], v[238:239]
	v_mov_b64_e32 v[4:5], v[240:241]
	v_mov_b64_e32 v[6:7], v[242:243]
	s_add_i32 s41, s42, s33
	s_ashr_i32 s30, s41, 3
	s_and_b32 s44, s36, 0x700
	s_ashr_i32 s31, s30, 31
	s_cmpk_lt_i32 s41, 0x400
	s_cselect_b64 s[6:7], -1, 0
	s_add_i32 s43, 0, 0x1a800
	v_add_u32_e32 v96, s43, v170
	ds_read_b64 v[96:97], v96
	v_lshlrev_b32_e32 v100, 16, v16
	v_and_b32_e32 v101, 0xffff0000, v16
	v_lshlrev_b32_e32 v98, 16, v17
	v_and_b32_e32 v99, 0xffff0000, v17
	v_lshlrev_b32_e32 v104, 16, v18
	v_and_b32_e32 v105, 0xffff0000, v18
	v_lshlrev_b32_e32 v102, 16, v19
	v_and_b32_e32 v103, 0xffff0000, v19
	s_waitcnt lgkmcnt(0)
	v_sub_f32_e32 v99, v99, v96
	v_sub_f32_e32 v98, v98, v96
	v_sub_f32_e32 v101, v101, v96
	v_sub_f32_e32 v100, v100, v96
	v_sub_f32_e32 v103, v103, v96
	v_sub_f32_e32 v102, v102, v96
	v_sub_f32_e32 v105, v105, v96
	v_sub_f32_e32 v104, v104, v96
	v_pk_mul_f32 v[100:101], v[96:97], v[100:101] op_sel:[1,0]
	v_pk_mul_f32 v[98:99], v[96:97], v[98:99] op_sel:[1,0]
	v_pk_mul_f32 v[104:105], v[96:97], v[104:105] op_sel:[1,0]
	v_pk_mul_f32 v[96:97], v[96:97], v[102:103] op_sel:[1,0]
	v_add_u32_e32 v214, v163, v171
	v_add_u32_e32 v118, s43, v172
	v_lshlrev_b32_e32 v106, 16, v20
	v_and_b32_e32 v107, 0xffff0000, v20
	v_lshlrev_b32_e32 v108, 16, v21
	v_and_b32_e32 v109, 0xffff0000, v21
	v_lshlrev_b32_e32 v110, 16, v22
	v_and_b32_e32 v111, 0xffff0000, v22
	v_lshlrev_b32_e32 v112, 16, v23
	v_and_b32_e32 v113, 0xffff0000, v23
	v_add_u32_e32 v121, s43, v173
	v_lshlrev_b32_e32 v114, 16, v24
	v_and_b32_e32 v115, 0xffff0000, v24
	v_lshlrev_b32_e32 v116, 16, v25
	v_and_b32_e32 v117, 0xffff0000, v25
	v_and_b32_e32 v119, 0xffff0000, v26
	v_lshlrev_b32_e32 v120, 16, v27
	s_lshl_b64 s[30:31], s[30:31], 7
	s_cmpk_gt_i32 s41, 0x3ff
	v_readlane_b32 s53, v249, 19
	v_readlane_b32 s54, v249, 20
	v_readlane_b32 s55, v249, 21
	v_readlane_b32 s56, v249, 22
	v_readlane_b32 s57, v249, 23
	v_readlane_b32 s58, v249, 24
	v_readlane_b32 s59, v249, 25
	s_waitcnt vmcnt(2)
	v_pk_fma_f32 v[98:99], v[10:11], v[98:99], v[14:15]
	v_pk_fma_f32 v[100:101], v[8:9], v[100:101], v[12:13]
	s_waitcnt vmcnt(0)
	v_pk_fma_f32 v[102:103], v[2:3], v[96:97], v[6:7]
	v_pk_fma_f32 v[104:105], v[0:1], v[104:105], v[4:5]
	v_cvt_pk_bf16_f32 v96, v100, v101
	v_cvt_pk_bf16_f32 v97, v98, v99
	v_cvt_pk_bf16_f32 v98, v104, v105
	v_cvt_pk_bf16_f32 v99, v102, v103
	ds_write_b128 v214, v[96:99] offset:34816
	ds_read_b64 v[96:97], v118
	v_lshlrev_b32_e32 v118, 16, v26
	s_waitcnt lgkmcnt(0)
	v_sub_f32_e32 v99, v109, v96
	v_sub_f32_e32 v98, v108, v96
	v_sub_f32_e32 v101, v107, v96
	v_sub_f32_e32 v100, v106, v96
	v_sub_f32_e32 v103, v113, v96
	v_sub_f32_e32 v102, v112, v96
	v_sub_f32_e32 v105, v111, v96
	v_sub_f32_e32 v104, v110, v96
	v_pk_mul_f32 v[100:101], v[96:97], v[100:101] op_sel:[1,0]
	v_pk_mul_f32 v[98:99], v[96:97], v[98:99] op_sel:[1,0]
	v_pk_mul_f32 v[104:105], v[96:97], v[104:105] op_sel:[1,0]
	v_pk_mul_f32 v[96:97], v[96:97], v[102:103] op_sel:[1,0]
	v_pk_fma_f32 v[98:99], v[10:11], v[98:99], v[14:15]
	v_pk_fma_f32 v[100:101], v[8:9], v[100:101], v[12:13]
	v_pk_fma_f32 v[102:103], v[2:3], v[96:97], v[6:7]
	v_pk_fma_f32 v[104:105], v[0:1], v[104:105], v[4:5]
	v_cvt_pk_bf16_f32 v96, v100, v101
	v_cvt_pk_bf16_f32 v97, v98, v99
	v_cvt_pk_bf16_f32 v98, v104, v105
	v_cvt_pk_bf16_f32 v99, v102, v103
	ds_write_b128 v214, v[96:99] offset:44032
	ds_read_b64 v[96:97], v121
	v_and_b32_e32 v102, 0xffff0000, v27
	v_or_b32_e32 v106, s44, v159
	v_lshlrev_b32_e32 v154, 1, v106
	s_waitcnt lgkmcnt(0)
	v_sub_f32_e32 v99, v117, v96
	v_sub_f32_e32 v98, v116, v96
	v_sub_f32_e32 v101, v115, v96
	v_sub_f32_e32 v100, v114, v96
	v_sub_f32_e32 v103, v102, v96
	v_sub_f32_e32 v102, v120, v96
	v_sub_f32_e32 v105, v119, v96
	v_sub_f32_e32 v104, v118, v96
	v_pk_mul_f32 v[100:101], v[96:97], v[100:101] op_sel:[1,0]
	v_pk_mul_f32 v[98:99], v[96:97], v[98:99] op_sel:[1,0]
	v_pk_mul_f32 v[104:105], v[96:97], v[104:105] op_sel:[1,0]
	v_pk_mul_f32 v[96:97], v[96:97], v[102:103] op_sel:[1,0]
	v_pk_fma_f32 v[98:99], v[10:11], v[98:99], v[14:15]
	v_pk_fma_f32 v[100:101], v[8:9], v[100:101], v[12:13]
	v_pk_fma_f32 v[102:103], v[2:3], v[96:97], v[6:7]
	v_pk_fma_f32 v[104:105], v[0:1], v[104:105], v[4:5]
	v_cvt_pk_bf16_f32 v96, v100, v101
	v_cvt_pk_bf16_f32 v97, v98, v99
	v_cvt_pk_bf16_f32 v98, v104, v105
	v_cvt_pk_bf16_f32 v99, v102, v103
	ds_write_b128 v214, v[96:99] offset:53248
	v_add_u32_e32 v96, s43, v174
	ds_read_b64 v[96:97], v96
	v_lshlrev_b32_e32 v100, 16, v28
	v_and_b32_e32 v101, 0xffff0000, v28
	v_lshlrev_b32_e32 v98, 16, v29
	v_and_b32_e32 v99, 0xffff0000, v29
	v_lshlrev_b32_e32 v104, 16, v30
	v_and_b32_e32 v105, 0xffff0000, v30
	v_lshlrev_b32_e32 v102, 16, v31
	v_and_b32_e32 v103, 0xffff0000, v31
	s_waitcnt lgkmcnt(0)
	v_sub_f32_e32 v99, v99, v96
	v_sub_f32_e32 v98, v98, v96
	v_sub_f32_e32 v101, v101, v96
	v_sub_f32_e32 v100, v100, v96
	v_sub_f32_e32 v103, v103, v96
	v_sub_f32_e32 v102, v102, v96
	v_sub_f32_e32 v105, v105, v96
	v_sub_f32_e32 v104, v104, v96
	v_pk_mul_f32 v[100:101], v[96:97], v[100:101] op_sel:[1,0]
	v_pk_mul_f32 v[98:99], v[96:97], v[98:99] op_sel:[1,0]
	v_pk_mul_f32 v[104:105], v[96:97], v[104:105] op_sel:[1,0]
	v_pk_mul_f32 v[96:97], v[96:97], v[102:103] op_sel:[1,0]
	v_pk_fma_f32 v[98:99], v[10:11], v[98:99], v[14:15]
	v_pk_fma_f32 v[100:101], v[8:9], v[100:101], v[12:13]
	v_pk_fma_f32 v[102:103], v[2:3], v[96:97], v[6:7]
	v_pk_fma_f32 v[104:105], v[0:1], v[104:105], v[4:5]
	v_cvt_pk_bf16_f32 v96, v100, v101
	v_cvt_pk_bf16_f32 v97, v98, v99
	v_cvt_pk_bf16_f32 v98, v104, v105
	v_cvt_pk_bf16_f32 v99, v102, v103
	ds_write_b128 v214, v[96:99] offset:62464
	v_add_u32_e32 v96, s43, v175
	ds_read_b64 v[96:97], v96
	v_lshlrev_b32_e32 v100, 16, v32
	v_and_b32_e32 v101, 0xffff0000, v32
	v_lshlrev_b32_e32 v98, 16, v33
	v_and_b32_e32 v99, 0xffff0000, v33
	v_lshlrev_b32_e32 v104, 16, v34
	v_and_b32_e32 v105, 0xffff0000, v34
	v_lshlrev_b32_e32 v102, 16, v35
	v_and_b32_e32 v103, 0xffff0000, v35
	s_waitcnt lgkmcnt(0)
	v_sub_f32_e32 v99, v99, v96
	v_sub_f32_e32 v98, v98, v96
	v_sub_f32_e32 v101, v101, v96
	v_sub_f32_e32 v100, v100, v96
	v_sub_f32_e32 v103, v103, v96
	v_sub_f32_e32 v102, v102, v96
	v_sub_f32_e32 v105, v105, v96
	v_sub_f32_e32 v104, v104, v96
	v_pk_mul_f32 v[100:101], v[96:97], v[100:101] op_sel:[1,0]
	v_pk_mul_f32 v[98:99], v[96:97], v[98:99] op_sel:[1,0]
	v_pk_mul_f32 v[104:105], v[96:97], v[104:105] op_sel:[1,0]
	v_pk_mul_f32 v[96:97], v[96:97], v[102:103] op_sel:[1,0]
	v_pk_fma_f32 v[98:99], v[10:11], v[98:99], v[14:15]
	v_pk_fma_f32 v[100:101], v[8:9], v[100:101], v[12:13]
	v_pk_fma_f32 v[102:103], v[2:3], v[96:97], v[6:7]
	v_pk_fma_f32 v[104:105], v[0:1], v[104:105], v[4:5]
	v_cvt_pk_bf16_f32 v96, v100, v101
	v_cvt_pk_bf16_f32 v97, v98, v99
	v_cvt_pk_bf16_f32 v98, v104, v105
	v_cvt_pk_bf16_f32 v99, v102, v103
	ds_write_b128 v212, v[96:99] offset:34816
	v_add_u32_e32 v96, s43, v176
	ds_read_b64 v[96:97], v96
	v_lshlrev_b32_e32 v100, 16, v36
	v_and_b32_e32 v101, 0xffff0000, v36
	v_lshlrev_b32_e32 v98, 16, v37
	v_and_b32_e32 v99, 0xffff0000, v37
	v_lshlrev_b32_e32 v104, 16, v38
	v_and_b32_e32 v105, 0xffff0000, v38
	v_lshlrev_b32_e32 v102, 16, v39
	v_and_b32_e32 v103, 0xffff0000, v39
	s_waitcnt lgkmcnt(0)
	v_sub_f32_e32 v99, v99, v96
	v_sub_f32_e32 v98, v98, v96
	v_sub_f32_e32 v101, v101, v96
	v_sub_f32_e32 v100, v100, v96
	v_sub_f32_e32 v103, v103, v96
	v_sub_f32_e32 v102, v102, v96
	v_sub_f32_e32 v105, v105, v96
	v_sub_f32_e32 v104, v104, v96
	v_pk_mul_f32 v[100:101], v[96:97], v[100:101] op_sel:[1,0]
	v_pk_mul_f32 v[98:99], v[96:97], v[98:99] op_sel:[1,0]
	v_pk_mul_f32 v[104:105], v[96:97], v[104:105] op_sel:[1,0]
	v_pk_mul_f32 v[96:97], v[96:97], v[102:103] op_sel:[1,0]
	v_pk_fma_f32 v[98:99], v[10:11], v[98:99], v[14:15]
	v_pk_fma_f32 v[100:101], v[8:9], v[100:101], v[12:13]
	v_pk_fma_f32 v[102:103], v[2:3], v[96:97], v[6:7]
	v_pk_fma_f32 v[104:105], v[0:1], v[104:105], v[4:5]
	v_cvt_pk_bf16_f32 v96, v100, v101
	v_cvt_pk_bf16_f32 v97, v98, v99
	v_cvt_pk_bf16_f32 v98, v104, v105
	v_cvt_pk_bf16_f32 v99, v102, v103
	ds_write_b128 v212, v[96:99] offset:44032
	v_add_u32_e32 v96, s43, v177
	ds_read_b64 v[96:97], v96
	v_lshlrev_b32_e32 v100, 16, v40
	v_and_b32_e32 v101, 0xffff0000, v40
	v_lshlrev_b32_e32 v98, 16, v41
	v_and_b32_e32 v99, 0xffff0000, v41
	v_lshlrev_b32_e32 v104, 16, v42
	v_and_b32_e32 v105, 0xffff0000, v42
	v_lshlrev_b32_e32 v102, 16, v43
	v_and_b32_e32 v103, 0xffff0000, v43
	s_waitcnt lgkmcnt(0)
	v_sub_f32_e32 v99, v99, v96
	v_sub_f32_e32 v98, v98, v96
	v_sub_f32_e32 v101, v101, v96
	v_sub_f32_e32 v100, v100, v96
	v_sub_f32_e32 v103, v103, v96
	v_sub_f32_e32 v102, v102, v96
	v_sub_f32_e32 v105, v105, v96
	v_sub_f32_e32 v104, v104, v96
	v_pk_mul_f32 v[100:101], v[96:97], v[100:101] op_sel:[1,0]
	v_pk_mul_f32 v[98:99], v[96:97], v[98:99] op_sel:[1,0]
	v_pk_mul_f32 v[104:105], v[96:97], v[104:105] op_sel:[1,0]
	v_pk_mul_f32 v[96:97], v[96:97], v[102:103] op_sel:[1,0]
	v_pk_fma_f32 v[98:99], v[10:11], v[98:99], v[14:15]
	v_pk_fma_f32 v[100:101], v[8:9], v[100:101], v[12:13]
	v_pk_fma_f32 v[102:103], v[2:3], v[96:97], v[6:7]
	v_pk_fma_f32 v[104:105], v[0:1], v[104:105], v[4:5]
	v_cvt_pk_bf16_f32 v96, v100, v101
	v_cvt_pk_bf16_f32 v97, v98, v99
	v_cvt_pk_bf16_f32 v98, v104, v105
	v_cvt_pk_bf16_f32 v99, v102, v103
	ds_write_b128 v212, v[96:99] offset:53248
	v_add_u32_e32 v96, s43, v178
	ds_read_b64 v[96:97], v96
	v_lshlrev_b32_e32 v100, 16, v44
	v_and_b32_e32 v101, 0xffff0000, v44
	v_lshlrev_b32_e32 v98, 16, v45
	v_and_b32_e32 v99, 0xffff0000, v45
	s_waitcnt lgkmcnt(0)
	v_sub_f32_e32 v99, v99, v96
	v_sub_f32_e32 v98, v98, v96
	v_sub_f32_e32 v101, v101, v96
	v_sub_f32_e32 v100, v100, v96
	v_lshlrev_b32_e32 v102, 16, v46
	v_and_b32_e32 v103, 0xffff0000, v46
	v_lshlrev_b32_e32 v104, 16, v47
	v_and_b32_e32 v105, 0xffff0000, v47
	v_pk_mul_f32 v[100:101], v[96:97], v[100:101] op_sel:[1,0]
	v_pk_mul_f32 v[98:99], v[96:97], v[98:99] op_sel:[1,0]
	v_pk_fma_f32 v[8:9], v[8:9], v[100:101], v[12:13]
	v_pk_fma_f32 v[10:11], v[10:11], v[98:99], v[14:15]
	v_sub_f32_e32 v13, v105, v96
	v_sub_f32_e32 v12, v104, v96
	v_sub_f32_e32 v15, v103, v96
	v_sub_f32_e32 v14, v102, v96
	v_pk_mul_f32 v[14:15], v[96:97], v[14:15] op_sel:[1,0]
	v_pk_mul_f32 v[12:13], v[96:97], v[12:13] op_sel:[1,0]
	s_nop 0
	v_pk_fma_f32 v[6:7], v[2:3], v[12:13], v[6:7]
	v_pk_fma_f32 v[2:3], v[0:1], v[14:15], v[4:5]
	v_cvt_pk_bf16_f32 v0, v8, v9
	v_cvt_pk_bf16_f32 v1, v10, v11
	v_cvt_pk_bf16_f32 v2, v2, v3
	v_cvt_pk_bf16_f32 v3, v6, v7
	ds_write_b128 v212, v[0:3] offset:62464
	v_lshl_add_u64 v[0:1], s[30:31], 0, v[130:131]
	v_lshlrev_b64 v[156:157], 12, v[0:1]
	s_cbranch_scc1 .LBB0_1970
	v_mov_b32_e32 v155, v133
	v_lshl_add_u64 v[0:1], s[14:15], 0, v[154:155]
	v_lshl_add_u64 v[0:1], v[0:1], 0, v[156:157]
	v_add_co_u32_e32 v2, vcc, 0x10000, v0
	s_nop 1
	v_addc_co_u32_e32 v3, vcc, 0, v1, vcc
	global_load_dwordx4 v[16:19], v[0:1], off nt
	global_load_dwordx4 v[20:23], v[2:3], off nt
	v_add_co_u32_e32 v2, vcc, 0x20000, v0
	s_nop 1
	v_addc_co_u32_e32 v3, vcc, 0, v1, vcc
	v_add_co_u32_e32 v4, vcc, 0x30000, v0
	s_nop 1
	v_addc_co_u32_e32 v5, vcc, 0, v1, vcc
	global_load_dwordx4 v[24:27], v[2:3], off nt
	global_load_dwordx4 v[28:31], v[4:5], off nt
	v_add_co_u32_e32 v2, vcc, 0x40000, v0
	s_nop 1
	v_addc_co_u32_e32 v3, vcc, 0, v1, vcc
	v_add_co_u32_e32 v4, vcc, 0x50000, v0
	s_nop 1
	v_addc_co_u32_e32 v5, vcc, 0, v1, vcc
	global_load_dwordx4 v[32:35], v[2:3], off nt
	global_load_dwordx4 v[36:39], v[4:5], off nt
	v_add_co_u32_e32 v2, vcc, 0x60000, v0
	s_nop 1
	v_addc_co_u32_e32 v3, vcc, 0, v1, vcc
	v_add_co_u32_e32 v0, vcc, 0x70000, v0
	s_nop 1
	v_addc_co_u32_e32 v1, vcc, 0, v1, vcc
	global_load_dwordx4 v[40:43], v[2:3], off nt
	global_load_dwordx4 v[44:47], v[0:1], off nt
	v_lshl_add_u64 v[0:1], s[30:31], 0, v[128:129]
	v_lshlrev_b64 v[0:1], 8, v[0:1]
	v_lshl_add_u64 v[0:1], v[136:137], 0, v[0:1]
	global_load_dwordx4 v[48:51], v[0:1], off offset:48
	global_load_dwordx4 v[52:55], v[0:1], off offset:32
	global_load_dwordx4 v[56:59], v[0:1], off offset:16
	global_load_dwordx4 v[60:63], v[0:1], off
